# MoE ticket: atomic at unit top not waited for, published to LDS at the K-loop exit before the aligned-epilogue barrier (reservation depth unchanged)
# baseline (speedup 1.0000x reference)
;     __device__ __forceinline__ void prefetch(int i) const { if (threadIdx.x == 0) tick[(base + i) & 3] = (int)__hip_atomic_fetch_add(qctr, 1u, __ATOMIC_RELAXED, __HIP_MEMORY_SCOPE_AGENT); }
; template <class Epi, class Sched>
; __device__ __forceinline__ void gemm_phase(LAS unsigned char* lds, const Sched& S, const Epi& E) {
;     ...
;         const bool has_next = S.next(ui + 1, nxt);
;         S.prefetch(ui + 2);
.LBB0_1232:
	s_and_saveexec_b64 s[18:19], s[0:1]
	s_cbranch_execz .LBB0_1236
	s_mov_b64 s[44:45], exec
	v_mbcnt_lo_u32_b32 v2, s44, 0
	v_mbcnt_hi_u32_b32 v2, s45, v2
	v_cmp_eq_u32_e32 vcc, 0, v2
	s_and_saveexec_b64 s[42:43], vcc
	s_cbranch_execz .LBB0_1235
	s_bcnt1_i32_b64 s5, s[44:45]
	v_mov_b32_e32 v3, s5
	global_atomic_add v250, v149, v3, s[6:7] sc0
.LBB0_1235:
	s_or_b64 exec, exec, s[42:43]
	s_xor_b32 s5, s39, 2
	s_add_i32 s5, s5, s24
	s_and_b32 s5, s5, 3
	s_lshl_b32 s5, s5, 2
	s_add_i32 s5, s5, 0
	s_add_i32 s5, s5, 0x21c00
	v_mov_b32_e32 v251, s5

; #define PG8_BAR __builtin_amdgcn_s_barrier()
; template <class Epi, class Sched>
; __device__ __forceinline__ void gemm_phase(LAS unsigned char* lds, const Sched& S, const Epi& E) {
;     ...
;         if constexpr (Epi::ALIGN) { if (wr == 0) PG8_BAR; }
.LBB0_1248:
	s_and_saveexec_b64 s[98:99], s[0:1]
	s_cbranch_execz .Ltk_p5
	s_waitcnt vmcnt(8)
	ds_write_b32 v251, v250
	s_waitcnt lgkmcnt(0)
.Ltk_p5:
	s_or_b64 exec, exec, s[98:99]
	s_cmpk_gt_u32 s47, 0xff
	s_cbranch_scc1 .Lp5_al
	s_barrier

;     __device__ __forceinline__ void prefetch(int i) const { if (threadIdx.x == 0) tick[(base + i) & 3] = (int)__hip_atomic_fetch_add(qctr, 1u, __ATOMIC_RELAXED, __HIP_MEMORY_SCOPE_AGENT); }
; template <class Epi, class Sched>
; __device__ __forceinline__ void gemm_phase(LAS unsigned char* lds, const Sched& S, const Epi& E) {
;     ...
;         const bool has_next = S.next(ui + 1, nxt);
;         S.prefetch(ui + 2);
.LBB0_1450:
	s_and_saveexec_b64 s[10:11], s[0:1]
	s_cbranch_execz .LBB0_1454
	s_mov_b64 s[50:51], exec
	v_mbcnt_lo_u32_b32 v2, s50, 0
	v_mbcnt_hi_u32_b32 v2, s51, v2
	v_cmp_eq_u32_e32 vcc, 0, v2
	s_and_saveexec_b64 s[48:49], vcc
	s_cbranch_execz .LBB0_1453
	s_bcnt1_i32_b64 s27, s[50:51]
	v_mov_b32_e32 v3, s27
	global_atomic_add v250, v147, v3, s[2:3] sc0
.LBB0_1453:
	s_or_b64 exec, exec, s[48:49]
	s_and_b32 s27, s45, 3
	s_xor_b32 s27, s27, 2
	s_lshl_b32 s27, s27, 2
	s_add_i32 s27, s27, 0
	s_add_i32 s27, s27, 0x21c00
	v_mov_b32_e32 v251, s27

; #define PG8_BAR __builtin_amdgcn_s_barrier()
; template <class Epi, class Sched>
; __device__ __forceinline__ void gemm_phase(LAS unsigned char* lds, const Sched& S, const Epi& E) {
;     ...
;         if constexpr (Epi::ALIGN) { if (wr == 0) PG8_BAR; }
.Ltk_p6:
	s_or_b64 exec, exec, s[98:99]
	s_andn2_b64 vcc, exec, s[16:17]
	s_cbranch_vccnz .LBB0_1463
	s_barrier

; __global__ void __launch_bounds__(NWAVES * 64, 2) fwd(Args args) {
	.amdhsa_kernel _Z3fwd4Args
		.amdhsa_group_segment_fixed_size 0
		.amdhsa_private_segment_fixed_size 0
		.amdhsa_kernarg_size 432
		.amdhsa_user_sgpr_count 2
		.amdhsa_user_sgpr_dispatch_ptr 0
		.amdhsa_user_sgpr_queue_ptr 0
		.amdhsa_user_sgpr_kernarg_segment_ptr 1
		.amdhsa_user_sgpr_dispatch_id 0
		.amdhsa_user_sgpr_kernarg_preload_length 0
		.amdhsa_user_sgpr_kernarg_preload_offset 0
		.amdhsa_user_sgpr_private_segment_size 0
		.amdhsa_uses_dynamic_stack 0
		.amdhsa_enable_private_segment 0
		.amdhsa_system_sgpr_workgroup_id_x 1
		.amdhsa_system_sgpr_workgroup_id_y 0
		.amdhsa_system_sgpr_workgroup_id_z 0
		.amdhsa_system_sgpr_workgroup_info 0
		.amdhsa_system_vgpr_workitem_id 0
		.amdhsa_next_free_vgpr 252
		.amdhsa_next_free_sgpr 102
		.amdhsa_accum_offset 252
		.amdhsa_reserve_vcc 1
		.amdhsa_float_round_mode_32 0
		.amdhsa_float_round_mode_16_64 0
		.amdhsa_float_denorm_mode_32 3
		.amdhsa_float_denorm_mode_16_64 3
		.amdhsa_dx10_clamp 1
		.amdhsa_ieee_mode 1
		.amdhsa_fp16_overflow 0
		.amdhsa_tg_split 0
		.amdhsa_exception_fp_ieee_invalid_op 0
		.amdhsa_exception_fp_denorm_src 0
		.amdhsa_exception_fp_ieee_div_zero 0
		.amdhsa_exception_fp_ieee_overflow 0
		.amdhsa_exception_fp_ieee_underflow 0
		.amdhsa_exception_fp_ieee_inexact 0
		.amdhsa_exception_int_div_zero 0
	.end_amdhsa_kernel

; __global__ void __launch_bounds__(NWAVES * 64, 2) fwd(Args args) {
amdhsa.kernels:
  - .agpr_count:     0
    .args:
      - .offset:         0
        .size:           176
        .value_kind:     by_value
      - .offset:         176
        .size:           4
        .value_kind:     hidden_block_count_x
      - .offset:         180
        .size:           4
        .value_kind:     hidden_block_count_y
      - .offset:         184
        .size:           4
        .value_kind:     hidden_block_count_z
      - .offset:         188
        .size:           2
        .value_kind:     hidden_group_size_x
      - .offset:         190
        .size:           2
        .value_kind:     hidden_group_size_y
      - .offset:         192
        .size:           2
        .value_kind:     hidden_group_size_z
      - .offset:         194
        .size:           2
        .value_kind:     hidden_remainder_x
      - .offset:         196
        .size:           2
        .value_kind:     hidden_remainder_y
      - .offset:         198
        .size:           2
        .value_kind:     hidden_remainder_z
      - .offset:         216
        .size:           8
        .value_kind:     hidden_global_offset_x
      - .offset:         224
        .size:           8
        .value_kind:     hidden_global_offset_y
      - .offset:         232
        .size:           8
        .value_kind:     hidden_global_offset_z
      - .offset:         240
        .size:           2
        .value_kind:     hidden_grid_dims
      - .offset:         296
        .size:           4
        .value_kind:     hidden_dynamic_lds_size
    .group_segment_fixed_size: 0
    .kernarg_segment_align: 8
    .kernarg_segment_size: 432
    .language:       OpenCL C
    .language_version:
      - 2
      - 0
    .max_flat_workgroup_size: 512
    .name:           _Z3fwd4Args
    .private_segment_fixed_size: 0
    .sgpr_count:     108
    .sgpr_spill_count: 40
    .symbol:         _Z3fwd4Args.kd
    .uniform_work_group_size: 1
    .uses_dynamic_stack: false
    .vgpr_count:     252
    .vgpr_spill_count: 0
    .wavefront_size: 64
